# v23 plus next-block gate loads issued one block ahead in the mLSTM state quad
# baseline (speedup 1.0000x reference)
; __device__ __forceinline__ int fresh_lane() { int l; asm volatile("v_mbcnt_lo_u32_b32 %0, -1, 0\n\tv_mbcnt_hi_u32_b32 %0, -1, %0" : "=v"(l)); __builtin_assume(l >= 0 && l < 64); return l; }
; __device__ __forceinline__ float logsigmoidf_(float x) { return fminf(x, 0.f) - log1pf(__expf(-fabsf(x))); }
; __device__ __forceinline__ void ml_gates(const Args& a, unsigned char* lds_g, int rowbase, int h, int tid) {
;     const int lane = fresh_lane(), w = __builtin_amdgcn_readfirstlane(tid >> 6), dir = w >> 2, c = w & 3;
;     const float* GT = (const float*)(a.ws + WS_GATES) + (size_t)(rowbase + 64 * c + lane) * 32;
;     const float ipre = GT[(dir * 2) * 8 + h], fpre = GT[(dir * 2 + 1) * 8 + h];
;     float bsum = logsigmoidf_(fpre);
; __device__ __forceinline__ void ml_state_quad(const Args& a, unsigned char* lds_g, int qu, int tid) {
;     ...
;         const int j = j0 + jj, su = seq * 8 + j;
;         const int rowbase = j == 0 ? b * CTXL : NCTX + b * SEQ + 256 * (dir ? 8 - j : j - 1);
;         ml_gates(a, lds_g, rowbase, h, tid);
.LBB0_266:
	s_add_i32 s6, s30, s49
	s_add_i32 s7, s6, 4
	s_and_b64 s[0:1], s[16:17], exec
	s_cselect_b32 s0, s29, s7
	s_lshl_b32 s0, s0, 8
	s_add_i32 s0, s31, s0
	s_cmp_eq_u32 s6, 4
	s_cselect_b32 s50, s33, s0
	v_readfirstlane_b32 s0, v180
	s_bfe_u32 s54, s0, 0x20006
	s_lshl_b32 s1, s54, 6
	v_mbcnt_lo_u32_b32 v0, -1, 0
	v_mbcnt_hi_u32_b32 v0, -1, v0
	s_lshr_b32 s51, s0, 8
	v_or_b32_e32 v2, s1, v0
	v_or_b32_e32 v2, s50, v2
	v_ashrrev_i32_e32 v3, 31, v2
	v_lshlrev_b64 v[2:3], 7, v[2:3]
	s_lshl_b32 s6, s51, 6
	v_lshl_add_u64 v[2:3], s[10:11], 0, v[2:3]
	s_or_b32 s14, s6, s48
	v_lshl_add_u64 v[2:3], v[2:3], 0, s[14:15]
	s_add_i32 s73, s30, s49
	s_add_i32 s73, s73, -1
	s_add_i32 s74, s73, 4
	s_add_i32 s75, s29, 1
	s_and_b64 s[76:77], s[16:17], exec
	s_cselect_b32 s74, s75, s74
	s_lshl_b32 s74, s74, 8
	s_add_i32 s74, s31, s74
	s_cmp_eq_u32 s73, 4
	s_cselect_b32 s74, s33, s74
	s_sub_i32 s74, s74, s50
	s_ashr_i32 s75, s74, 31
	s_lshl_b64 s[74:75], s[74:75], 7
	v_lshl_add_u64 v[136:137], v[2:3], 0, s[74:75]
	s_cmp_eq_u32 s49, 4
	s_cbranch_scc0 .Lqg_copy
	global_load_dword v50, v[2:3], off offset:32
	s_nop 0
	global_load_dword v2, v[2:3], off
	s_branch .Lqg_join
.Lqg_copy:
	s_waitcnt vmcnt(9)
	v_mov_b32_e32 v50, v138
	v_mov_b32_e32 v2, v139
; __device__ __forceinline__ int fresh_lane() { int l; asm volatile("v_mbcnt_lo_u32_b32 %0, -1, 0\n\tv_mbcnt_hi_u32_b32 %0, -1, %0" : "=v"(l)); __builtin_assume(l >= 0 && l < 64); return l; }
; __device__ __forceinline__ float logsigmoidf_(float x) { return fminf(x, 0.f) - log1pf(__expf(-fabsf(x))); }
; __device__ __forceinline__ void ml_gates(const Args& a, unsigned char* lds_g, int rowbase, int h, int tid) {
;     const int lane = fresh_lane(), w = __builtin_amdgcn_readfirstlane(tid >> 6), dir = w >> 2, c = w & 3;
;     const float* GT = (const float*)(a.ws + WS_GATES) + (size_t)(rowbase + 64 * c + lane) * 32;
;     const float ipre = GT[(dir * 2) * 8 + h], fpre = GT[(dir * 2 + 1) * 8 + h];
;     float bsum = logsigmoidf_(fpre);
;     if (dir == 0) {
; #pragma unroll
;         for (int o = 1; o < 64; o <<= 1) { const float t = __shfl_up(bsum, o); if (lane >= o) bsum += t; }
;     } else {
; #pragma unroll
;         for (int o = 1; o < 64; o <<= 1) { const float t = __shfl_down(bsum, o); if (lane + o < 64) bsum += t; }
;     }
; template <bool OUT, bool PASS2>
; __device__ __forceinline__ void ml_block(const Args& a, unsigned char* lds_g, int rowbase, int h, int dir, f32x4 (&st)[9], int tid) {
;     ...
;     ML_LOADC(dir ? 3 : 0);
.Lqg_join:
	v_or_b32_e32 v181, s50, v51
	v_mov_b32_e32 v183, 0
	v_or_b32_e32 v182, s35, v181
	v_lshlrev_b32_e32 v182, 11, v182
	v_lshl_add_u64 v[120:121], v[46:47], 0, v[182:183]
	v_lshl_add_u64 v[122:123], v[48:49], 0, v[182:183]
	global_load_dwordx4 v[184:187], v[120:121], off offset:16
	global_load_dwordx4 v[188:191], v[120:121], off
	global_load_dwordx4 v[192:195], v[122:123], off
	global_load_dwordx4 v[196:199], v[122:123], off offset:16
	v_or_b32_e32 v182, s37, v181
	v_lshlrev_b32_e32 v182, 11, v182
	v_lshl_add_u64 v[124:125], v[46:47], 0, v[182:183]
	v_lshl_add_u64 v[126:127], v[48:49], 0, v[182:183]
	global_load_dwordx4 v[200:203], v[124:125], off offset:16
	global_load_dwordx4 v[204:207], v[124:125], off
	global_load_dwordx4 v[208:211], v[126:127], off
	global_load_dwordx4 v[212:215], v[126:127], off offset:16
	v_or_b32_e32 v182, s40, v181
	v_lshlrev_b32_e32 v182, 11, v182
	v_lshl_add_u64 v[128:129], v[46:47], 0, v[182:183]
	v_lshl_add_u64 v[130:131], v[48:49], 0, v[182:183]
	global_load_dwordx4 v[216:219], v[128:129], off offset:16
	global_load_dwordx4 v[220:223], v[128:129], off
	global_load_dwordx4 v[224:227], v[130:131], off
	global_load_dwordx4 v[228:231], v[130:131], off offset:16
	v_or_b32_e32 v182, s43, v181
	v_lshlrev_b32_e32 v182, 11, v182
	v_lshl_add_u64 v[132:133], v[46:47], 0, v[182:183]
	v_lshl_add_u64 v[134:135], v[48:49], 0, v[182:183]
	global_load_dwordx4 v[232:235], v[132:133], off offset:16
	global_load_dwordx4 v[236:239], v[132:133], off
	global_load_dwordx4 v[240:243], v[134:135], off
	global_load_dwordx4 v[244:247], v[134:135], off offset:16
	global_load_dword v138, v[136:137], off offset:32
	global_load_dword v139, v[136:137], off
	s_mov_b64 s[6:7], -1
	s_cmpk_lt_u32 s0, 0x100
	s_waitcnt vmcnt(18)
	v_mul_f32_e64 v3, |v50|, s23
	v_exp_f32_e32 v3, v3
	v_max_f32_e32 v50, v50, v50
	v_min_f32_e32 v50, 0, v50
	v_add_f32_e32 v72, 1.0, v3
	v_add_f32_e32 v73, -1.0, v72
	v_frexp_mant_f32_e32 v78, v72
	v_cvt_f64_f32_e32 v[70:71], v72
	v_sub_f32_e32 v79, v73, v72
	v_frexp_exp_i32_f64_e32 v70, v[70:71]
	v_cmp_gt_f32_e32 vcc, s24, v78
	v_sub_f32_e32 v73, v3, v73
	v_add_f32_e32 v71, 1.0, v79
	v_subbrev_co_u32_e32 v70, vcc, 0, v70, vcc
	v_add_f32_e32 v71, v73, v71
	v_sub_u32_e32 v73, 0, v70
	v_cvt_f32_i32_e32 v70, v70
	v_ldexp_f32 v72, v72, v73
	v_ldexp_f32 v71, v71, v73
	v_add_f32_e32 v73, -1.0, v72
	v_add_f32_e32 v78, 1.0, v72
	v_add_f32_e32 v79, 1.0, v73
	v_add_f32_e32 v80, -1.0, v78
	v_sub_f32_e32 v79, v72, v79
	v_sub_f32_e32 v72, v72, v80
	v_mul_f32_e32 v80, 0x3f317218, v70
	v_add_f32_e32 v79, v71, v79
	v_add_f32_e32 v71, v71, v72
	v_fma_f32 v72, v70, s25, -v80
	v_add_f32_e32 v81, v73, v79
	v_add_f32_e32 v82, v78, v71
	v_fmac_f32_e32 v72, 0xb102e308, v70
	v_sub_f32_e32 v70, v81, v73
	v_sub_f32_e32 v73, v82, v78
	v_rcp_f32_e32 v78, v82
	v_add_f32_e32 v83, v80, v72
	v_sub_f32_e32 v71, v71, v73
	v_sub_f32_e32 v73, v83, v80
	v_sub_f32_e32 v72, v72, v73
	v_mul_f32_e32 v73, v81, v78
	v_sub_f32_e32 v70, v79, v70
	v_mul_f32_e32 v79, v82, v73
	v_fma_f32 v80, v73, v82, -v79
	v_fmac_f32_e32 v80, v73, v71
	v_add_f32_e32 v84, v79, v80
	v_sub_f32_e32 v85, v81, v84
	v_sub_f32_e32 v79, v84, v79
	v_sub_f32_e32 v81, v81, v85
	v_sub_f32_e32 v79, v79, v80
	v_sub_f32_e32 v80, v81, v84
	v_add_f32_e32 v70, v70, v80
	v_add_f32_e32 v70, v79, v70
	v_add_f32_e32 v79, v85, v70
	v_mul_f32_e32 v80, v78, v79
	v_sub_f32_e32 v81, v85, v79
	v_mul_f32_e32 v84, v82, v80
	v_add_f32_e32 v70, v70, v81
	v_add_f32_e32 v81, v73, v80
	v_fma_f32 v82, v80, v82, -v84
	v_sub_f32_e32 v73, v81, v73
	v_fmac_f32_e32 v82, v80, v71
	v_sub_f32_e32 v71, v80, v73
	v_add_f32_e32 v73, v84, v82
	v_sub_f32_e32 v80, v73, v84
	v_sub_f32_e32 v84, v79, v73
	v_sub_f32_e32 v79, v79, v84
	v_sub_f32_e32 v73, v79, v73
	v_sub_f32_e32 v80, v80, v82
	v_add_f32_e32 v70, v70, v73
	v_add_f32_e32 v70, v80, v70
	v_add_f32_e32 v70, v84, v70
	v_mul_f32_e32 v70, v78, v70
	v_add_f32_e32 v70, v71, v70
	v_add_f32_e32 v71, v81, v70
	v_mul_f32_e32 v73, v71, v71
	v_fmamk_f32 v80, v73, 0x3e9b6dac, v60
	v_sub_f32_e32 v78, v71, v81
	v_ldexp_f32 v79, v71, 1
	v_mul_f32_e32 v71, v71, v73
	v_fmaak_f32 v73, v73, v80, 0x3f2aaada
	v_mul_f32_e32 v71, v71, v73
	v_add_f32_e32 v73, v79, v71
	v_sub_f32_e32 v70, v70, v78
	v_sub_f32_e32 v78, v73, v79
	v_ldexp_f32 v70, v70, 1
	v_sub_f32_e32 v71, v71, v78
	v_add_f32_e32 v70, v70, v71
	v_add_f32_e32 v71, v73, v70
	v_sub_f32_e32 v73, v71, v73
	v_add_f32_e32 v78, v83, v71
	v_sub_f32_e32 v70, v70, v73
	v_sub_f32_e32 v73, v78, v83
	v_sub_f32_e32 v79, v78, v73
	v_sub_f32_e32 v71, v71, v73
	v_add_f32_e32 v73, v72, v70
	v_sub_f32_e32 v79, v83, v79
	v_sub_f32_e32 v80, v73, v72
	v_add_f32_e32 v71, v71, v79
	v_sub_f32_e32 v79, v73, v80
	v_sub_f32_e32 v70, v70, v80
	v_sub_f32_e32 v72, v72, v79
	v_add_f32_e32 v71, v73, v71
	v_add_f32_e32 v70, v70, v72
	v_add_f32_e32 v72, v78, v71
	v_sub_f32_e32 v73, v72, v78
	v_sub_f32_e32 v71, v71, v73
	v_add_f32_e32 v70, v70, v71
	v_add_f32_e32 v70, v72, v70
	v_cmp_neq_f32_e32 vcc, s26, v3
	s_nop 1
	v_cndmask_b32_e32 v70, v61, v70, vcc
	v_cmp_ngt_f32_e32 vcc, -1.0, v3
	s_nop 1
	v_cndmask_b32_e32 v70, v62, v70, vcc
	v_cmp_neq_f32_e32 vcc, -1.0, v3
	s_nop 1
	v_cndmask_b32_e32 v70, v63, v70, vcc
	v_cmp_lt_f32_e64 vcc, |v3|, s27
	s_nop 1
	v_cndmask_b32_e32 v3, v70, v3, vcc
	v_sub_f32_e32 v3, v50, v3
	v_cmp_gt_u32_e32 vcc, 32, v0
	s_cbranch_scc1 .LBB0_268
	v_and_b32_e32 v50, 63, v64
	v_cmp_ne_u32_e64 s[6:7], 63, v50
	s_nop 1
	v_addc_co_u32_e64 v70, s[6:7], 0, v64, s[6:7]
	v_lshlrev_b32_e32 v70, 2, v70
	ds_bpermute_b32 v70, v70, v3
	v_cmp_eq_u32_e64 s[6:7], 63, v0
	s_waitcnt lgkmcnt(0)
	v_add_f32_e32 v70, v3, v70
	v_cndmask_b32_e64 v70, v70, v3, s[6:7]
	v_cmp_gt_u32_e64 s[6:7], 62, v50
	s_nop 1
	v_cndmask_b32_e64 v71, 0, 2, s[6:7]
	v_add_lshl_u32 v71, v71, v64, 2
	ds_bpermute_b32 v71, v71, v70
	v_cmp_gt_u32_e64 s[6:7], 62, v0
	s_waitcnt lgkmcnt(0)
	v_add_f32_e32 v71, v70, v71
	v_cndmask_b32_e64 v70, v70, v71, s[6:7]
	v_cmp_gt_u32_e64 s[6:7], 60, v50
	s_nop 1
	v_cndmask_b32_e64 v71, 0, 4, s[6:7]
	v_add_lshl_u32 v71, v71, v64, 2
	ds_bpermute_b32 v71, v71, v70
	v_cmp_gt_u32_e64 s[6:7], 60, v0
	s_waitcnt lgkmcnt(0)
	v_add_f32_e32 v71, v70, v71
	v_cndmask_b32_e64 v70, v70, v71, s[6:7]
	v_cmp_gt_u32_e64 s[6:7], 56, v50
	s_nop 1
	v_cndmask_b32_e64 v71, 0, 8, s[6:7]
	v_add_lshl_u32 v71, v71, v64, 2
	ds_bpermute_b32 v71, v71, v70
	v_cmp_gt_u32_e64 s[6:7], 56, v0
	s_waitcnt lgkmcnt(0)
	v_add_f32_e32 v71, v70, v71
	v_cndmask_b32_e64 v70, v70, v71, s[6:7]
	v_cmp_gt_u32_e64 s[6:7], 48, v50
	s_nop 1
	v_cndmask_b32_e64 v50, 0, 16, s[6:7]
	v_add_lshl_u32 v50, v50, v64, 2
	ds_bpermute_b32 v50, v50, v70
	v_cmp_gt_u32_e64 s[6:7], 48, v0
	s_waitcnt lgkmcnt(0)
	v_add_f32_e32 v50, v70, v50
	v_cndmask_b32_e64 v50, v70, v50, s[6:7]
	ds_bpermute_b32 v70, v65, v50
	s_mov_b64 s[6:7], 0
	s_waitcnt lgkmcnt(0)
	v_add_f32_e32 v70, v50, v70
	v_cndmask_b32_e32 v50, v50, v70, vcc

; template <bool OUT, bool PASS2>
; __device__ __forceinline__ void ml_block(const Args& a, unsigned char* lds_g, int rowbase, int h, int dir, f32x4 (&st)[9], int tid) {
;     ...
;         {
;             const int t = st_t, pc = st_pc;
;             const float e = eu[64 * c + t];
;             *(v4u*)(Ki + t * ML_STRIDE + 16 * pc) = k0; *(v4u*)(Ki + t * ML_STRIDE + 16 * pc + 8) = k1;
;             if (OUT) { *(v4u*)(Qi + t * ML_STRIDE + 16 * pc) = q0; *(v4u*)(Qi + t * ML_STRIDE + 16 * pc + 8) = q1; }
;             const unsigned vv[8] = {v0.x, v0.y, v0.z, v0.w, v1.x, v1.y, v1.z, v1.w}; unsigned o[8];
; #pragma unroll
;             for (int i = 0; i < 8; ++i) o[i] = pk2(bflo(vv[i]) * e, bfhi(vv[i]) * e);
;             *(v4u*)(Vi + t * ML_STRIDE + 16 * pc) = (v4u){o[0], o[1], o[2], o[3]}; *(v4u*)(Vi + t * ML_STRIDE + 16 * pc + 8) = (v4u){o[4], o[5], o[6], o[7]};
;             if (pc == 0) { *(v4u*)(AUGi + t * 16) = (v4u){f2bf(e), 0u, 0u, 0u}; *(v4u*)(AUGi + t * 16 + 8) = (v4u){0u, 0u, 0u, 0u}; }
;         }
;         WG_BAR();
;         if (ci < 3) ML_LOADC(dir ? 2 - ci : ci + 1);
;         f32x4 X[5]; float hval[4][4];
;         if (OUT) {
;             bf16x8_t qf[4];
; #pragma unroll
;             for (int ks = 0; ks < 4; ++ks) qf[ks] = frag_row(Qi, 16 * ti, 32 * ks, fr, fq);
;             bf16x8_t P[2]; bool pv[2];
; #pragma unroll
;             for (int pp = 0; pp < 2; ++pp) {
;                 f32x4 d[2];
; #pragma unroll
;                 for (int hh = 0; hh < 2; ++hh) { const int si = 2 * pp + hh; d[hh] = (f32x4){0.f, 0.f, 0.f, 0.f};
;                     const bool valid = dir ? (si >= ti) : (si <= ti);
;                     if (valid) {
; #pragma unroll
;                         for (int ks = 0; ks < 4; ++ks) d[hh] = __builtin_amdgcn_mfma_f32_16x16x32_bf16(frag_row(Ki, 16 * si, 32 * ks, fr, fq), qf[ks], d[hh], 0, 0, 0);
;                         if (si == ti) {
; #pragma unroll
;                             for (int r = 0; r < 4; ++r) { const bool keep = dir ? (4 * fq + r >= fr) : (4 * fq + r <= fr); d[hh][r] = keep ? d[hh][r] : 0.f; } } } }
;                 pv[pp] = dir ? (2 * pp + 1 >= ti) : (2 * pp <= ti);
;                 const unsigned p0 = pk2(d[0][0], d[0][1]), p1 = pk2(d[0][2], d[0][3]), p2 = pk2(d[1][0], d[1][1]), p3 = pk2(d[1][2], d[1][3]);
;                 P[pp] = __builtin_bit_cast(bf16x8_t, (v4u){p0, p1, p2, p3});
;             }
.LBB0_272:
	s_or_b64 exec, exec, s[0:1]
	v_or_b32_e32 v73, s50, v51
	s_waitcnt lgkmcnt(2)
	v_or_b32_e32 v2, s35, v73
	v_ashrrev_i32_e32 v3, 31, v2
	v_lshlrev_b64 v[2:3], 11, v[2:3]
	s_waitcnt lgkmcnt(0)
	s_barrier
	v_lshl_add_u64 v[70:71], v[46:47], 0, v[2:3]
	v_lshl_add_u64 v[2:3], v[48:49], 0, v[2:3]
	v_add_u32_e32 v0, s36, v69
	ds_read_b32 v0, v0
	v_readfirstlane_b32 s6, v180
	s_waitcnt vmcnt(14)
	v_mov_b64_e32 v[78:79], v[184:185]
	v_mov_b64_e32 v[80:81], v[186:187]
	v_mov_b64_e32 v[82:83], v[188:189]
	v_mov_b64_e32 v[84:85], v[190:191]
	v_mov_b64_e32 v[86:87], v[192:193]
	v_mov_b64_e32 v[88:89], v[194:195]
	v_mov_b64_e32 v[90:91], v[196:197]
	v_mov_b64_e32 v[92:93], v[198:199]
	ds_write_b128 v53, v[82:85] offset:17408
	ds_write_b128 v53, v[78:81] offset:17424
	v_lshlrev_b32_e32 v2, 16, v86
	v_and_b32_e32 v3, 0xffff0000, v86
	v_lshlrev_b32_e32 v70, 16, v87
	v_and_b32_e32 v71, 0xffff0000, v87
	v_lshlrev_b32_e32 v78, 16, v88
	v_and_b32_e32 v79, 0xffff0000, v88
	v_lshlrev_b32_e32 v80, 16, v89
	v_and_b32_e32 v81, 0xffff0000, v89
	v_lshlrev_b32_e32 v82, 16, v90
	v_and_b32_e32 v83, 0xffff0000, v90
	v_lshlrev_b32_e32 v84, 16, v91
	v_and_b32_e32 v85, 0xffff0000, v91
	v_lshlrev_b32_e32 v86, 16, v92
	v_and_b32_e32 v87, 0xffff0000, v92
	v_lshlrev_b32_e32 v88, 16, v93
	v_and_b32_e32 v89, 0xffff0000, v93
	s_waitcnt lgkmcnt(2)
	v_pk_mul_f32 v[2:3], v[0:1], v[2:3] op_sel_hi:[0,1]
	v_pk_mul_f32 v[70:71], v[0:1], v[70:71] op_sel_hi:[0,1]
	v_pk_mul_f32 v[90:91], v[0:1], v[78:79] op_sel_hi:[0,1]
	v_pk_mul_f32 v[92:93], v[0:1], v[80:81] op_sel_hi:[0,1]
	v_pk_mul_f32 v[82:83], v[0:1], v[82:83] op_sel_hi:[0,1]
	v_pk_mul_f32 v[84:85], v[0:1], v[84:85] op_sel_hi:[0,1]
	v_pk_mul_f32 v[86:87], v[0:1], v[86:87] op_sel_hi:[0,1]
	v_pk_mul_f32 v[88:89], v[0:1], v[88:89] op_sel_hi:[0,1]
	v_cvt_pk_bf16_f32 v78, v2, v3
	v_cvt_pk_bf16_f32 v79, v70, v71
	v_cvt_pk_bf16_f32 v80, v90, v91
	v_cvt_pk_bf16_f32 v81, v92, v93
	v_cvt_pk_bf16_f32 v82, v82, v83
	v_cvt_pk_bf16_f32 v83, v84, v85
	v_cvt_pk_bf16_f32 v84, v86, v87
	v_cvt_pk_bf16_f32 v85, v88, v89
	ds_write_b128 v53, v[78:81] offset:34816
	ds_write_b128 v53, v[82:85] offset:34832
	s_and_saveexec_b64 s[0:1], s[8:9]
	s_cbranch_execz .LBB0_274
	v_bfe_u32 v2, v0, 16, 1
	v_add3_u32 v0, v0, v2, s28
	v_lshrrev_b32_e32 v0, 16, v0
	v_mov_b32_e32 v2, v1
	v_mov_b32_e32 v3, v1
	ds_write_b128 v66, v[0:3] offset:52224
	ds_write_b128 v66, v[74:77] offset:52240
.LBB0_274:
	s_or_b64 exec, exec, s[0:1]
	s_lshr_b32 s0, s6, 1
	s_and_b32 s0, s0, 0x7fffffe0
	v_add_u32_e32 v0, s0, v54
	s_waitcnt lgkmcnt(0)
	s_barrier
	v_lshl_add_u32 v71, v55, 1, v0
	ds_read_b64_tr_b16 v[78:79], v71 offset:17408
	ds_read_b64_tr_b16 v[80:81], v71 offset:18496
	ds_read_b64_tr_b16 v[82:83], v56 offset:34816
	ds_read_b64_tr_b16 v[86:87], v56 offset:34848
	ds_read_b64_tr_b16 v[90:91], v56 offset:34880
	ds_read_b64_tr_b16 v[94:95], v56 offset:34912
	ds_read_b64_tr_b16 v[84:85], v56 offset:35904
	ds_read_b64_tr_b16 v[88:89], v56 offset:35936
	ds_read_b64_tr_b16 v[92:93], v56 offset:35968
	ds_read_b64_tr_b16 v[96:97], v56 offset:36000
	v_lshl_add_u32 v72, v58, 1, v0
	ds_read_b64_tr_b16 v[98:99], v72 offset:17408
	ds_read_b64_tr_b16 v[100:101], v72 offset:18496
	s_waitcnt lgkmcnt(5)
	v_mfma_f32_16x16x32_bf16 v[36:39], v[78:81], v[82:85], v[36:39]
	v_add_u32_e32 v70, v54, v57
	v_mov_b32_e32 v0, s38
	s_waitcnt lgkmcnt(4)
	v_mfma_f32_16x16x32_bf16 v[32:35], v[78:81], v[86:89], v[32:35]
	s_waitcnt lgkmcnt(3)
	v_mfma_f32_16x16x32_bf16 v[28:31], v[78:81], v[90:93], v[28:31]
	s_waitcnt lgkmcnt(2)
	v_mfma_f32_16x16x32_bf16 v[24:27], v[78:81], v[94:97], v[24:27]
	ds_read_b64_tr_b16 v[84:85], v56 offset:36032
	ds_read_b64_tr_b16 v[82:83], v56 offset:34944
	ds_read_b64_tr_b16 v[86:87], v56 offset:34976
	ds_read_b64_tr_b16 v[90:91], v56 offset:35008
	ds_read_b64_tr_b16 v[94:95], v56 offset:35040
	ds_read_b64_tr_b16 v[88:89], v56 offset:36064
	ds_read_b64_tr_b16 v[92:93], v56 offset:36096
	ds_read_b64_tr_b16 v[96:97], v56 offset:36128
	s_waitcnt lgkmcnt(6)
	v_mfma_f32_16x16x32_bf16 v[20:23], v[78:81], v[82:85], v[20:23]
	s_waitcnt lgkmcnt(2)
	v_mfma_f32_16x16x32_bf16 v[82:85], v[78:81], v[86:89], v[16:19]
	s_waitcnt lgkmcnt(1)
	v_mfma_f32_16x16x32_bf16 v[86:89], v[78:81], v[90:93], v[12:15]
	s_waitcnt lgkmcnt(0)
	v_mfma_f32_16x16x32_bf16 v[90:93], v[78:81], v[94:97], v[8:11]
	s_nop 2
	ds_read_b64_tr_b16 v[8:9], v70 offset:52224
	ds_read_b64_tr_b16 v[10:11], v70 offset:52352
	ds_read_b64_tr_b16 v[94:95], v67 offset:52224
	ds_read_b64_tr_b16 v[96:97], v67 offset:52352
	s_waitcnt lgkmcnt(2)
	v_mfma_f32_16x16x32_bf16 v[78:81], v[78:81], v[8:11], v[4:7]
	s_nop 2
	ds_read_b64_tr_b16 v[4:5], v59 offset:35904
	ds_read_b64_tr_b16 v[2:3], v59 offset:34816
	ds_read_b64_tr_b16 v[6:7], v59 offset:34848
	ds_read_b64_tr_b16 v[12:13], v59 offset:34880
	ds_read_b64_tr_b16 v[16:17], v59 offset:34912
	ds_read_b64_tr_b16 v[8:9], v59 offset:35936
	ds_read_b64_tr_b16 v[14:15], v59 offset:35968
	ds_read_b64_tr_b16 v[18:19], v59 offset:36000
	s_waitcnt lgkmcnt(6)
	v_mfma_f32_16x16x32_bf16 v[36:39], v[98:101], v[2:5], v[36:39]
	v_or_b32_e32 v2, s37, v73
	v_ashrrev_i32_e32 v3, 31, v2
	v_lshlrev_b64 v[2:3], 11, v[2:3]
	v_lshl_add_u64 v[118:119], v[48:49], 0, v[2:3]
	v_lshl_add_u64 v[2:3], v[46:47], 0, v[2:3]
	s_waitcnt lgkmcnt(2)
	v_mfma_f32_16x16x32_bf16 v[8:11], v[98:101], v[6:9], v[32:35]
	s_waitcnt lgkmcnt(0)
	v_mfma_f32_16x16x32_bf16 v[16:19], v[98:101], v[16:19], v[24:27]
	ds_read_b64_tr_b16 v[4:5], v59 offset:36032
	ds_read_b64_tr_b16 v[2:3], v59 offset:34944
	s_nop 0
	ds_read_b64_tr_b16 v[24:25], v59 offset:34976
	ds_read_b64_tr_b16 v[32:33], v59 offset:35008
	ds_read_b64_tr_b16 v[110:111], v59 offset:35040
	ds_read_b64_tr_b16 v[26:27], v59 offset:36064
	ds_read_b64_tr_b16 v[34:35], v59 offset:36096
	ds_read_b64_tr_b16 v[112:113], v59 offset:36128
	ds_read_b32 v50, v0
	v_mfma_f32_16x16x32_bf16 v[12:15], v[98:101], v[12:15], v[28:31]
	s_waitcnt lgkmcnt(7)
	v_mfma_f32_16x16x32_bf16 v[28:31], v[98:101], v[2:5], v[20:23]
	v_add_u32_e32 v2, s39, v69
	s_waitcnt lgkmcnt(3)
	v_mfma_f32_16x16x32_bf16 v[4:7], v[98:101], v[24:27], v[82:85]
	s_nop 2
	s_waitcnt lgkmcnt(0)
	s_barrier
; template <bool OUT, bool PASS2>
; __device__ __forceinline__ void ml_block(const Args& a, unsigned char* lds_g, int rowbase, int h, int dir, f32x4 (&st)[9], int tid) {
;     ...
;         {
;             const int t = st_t, pc = st_pc;
;             const float e = eu[64 * c + t];
;             *(v4u*)(Ki + t * ML_STRIDE + 16 * pc) = k0; *(v4u*)(Ki + t * ML_STRIDE + 16 * pc + 8) = k1;
;             if (OUT) { *(v4u*)(Qi + t * ML_STRIDE + 16 * pc) = q0; *(v4u*)(Qi + t * ML_STRIDE + 16 * pc + 8) = q1; }
;             const unsigned vv[8] = {v0.x, v0.y, v0.z, v0.w, v1.x, v1.y, v1.z, v1.w}; unsigned o[8];
; #pragma unroll
;             for (int i = 0; i < 8; ++i) o[i] = pk2(bflo(vv[i]) * e, bfhi(vv[i]) * e);
;             *(v4u*)(Vi + t * ML_STRIDE + 16 * pc) = (v4u){o[0], o[1], o[2], o[3]}; *(v4u*)(Vi + t * ML_STRIDE + 16 * pc + 8) = (v4u){o[4], o[5], o[6], o[7]};
;             if (pc == 0) { *(v4u*)(AUGi + t * 16) = (v4u){f2bf(e), 0u, 0u, 0u}; *(v4u*)(AUGi + t * 16 + 8) = (v4u){0u, 0u, 0u, 0u}; }
;         }
;         WG_BAR();
;         if (ci < 3) ML_LOADC(dir ? 2 - ci : ci + 1);
;         f32x4 X[5]; float hval[4][4];
;         if (OUT) {
;             bf16x8_t qf[4];
; #pragma unroll
;             for (int ks = 0; ks < 4; ++ks) qf[ks] = frag_row(Qi, 16 * ti, 32 * ks, fr, fq);
;             bf16x8_t P[2]; bool pv[2];
; #pragma unroll
;             for (int pp = 0; pp < 2; ++pp) {
;                 f32x4 d[2];
; #pragma unroll
;                 for (int hh = 0; hh < 2; ++hh) { const int si = 2 * pp + hh; d[hh] = (f32x4){0.f, 0.f, 0.f, 0.f};
;                     const bool valid = dir ? (si >= ti) : (si <= ti);
;                     if (valid) {
; #pragma unroll
;                         for (int ks = 0; ks < 4; ++ks) d[hh] = __builtin_amdgcn_mfma_f32_16x16x32_bf16(frag_row(Ki, 16 * si, 32 * ks, fr, fq), qf[ks], d[hh], 0, 0, 0);
;                         if (si == ti) {
; #pragma unroll
;                             for (int r = 0; r < 4; ++r) { const bool keep = dir ? (4 * fq + r >= fr) : (4 * fq + r <= fr); d[hh][r] = keep ? d[hh][r] : 0.f; } } } }
;                 pv[pp] = dir ? (2 * pp + 1 >= ti) : (2 * pp <= ti);
;                 const unsigned p0 = pk2(d[0][0], d[0][1]), p1 = pk2(d[0][2], d[0][3]), p2 = pk2(d[1][0], d[1][1]), p3 = pk2(d[1][2], d[1][3]);
;                 P[pp] = __builtin_bit_cast(bf16x8_t, (v4u){p0, p1, p2, p3});
;             }
	ds_read_b32 v0, v2
	v_mfma_f32_16x16x32_bf16 v[24:27], v[98:101], v[94:97], v[78:81]
	s_waitcnt vmcnt(10)
	v_mov_b64_e32 v[102:103], v[200:201]
	v_mov_b64_e32 v[104:105], v[202:203]
	v_mov_b64_e32 v[106:107], v[204:205]
	v_mov_b64_e32 v[108:109], v[206:207]
	v_mov_b64_e32 v[114:115], v[208:209]
	v_mov_b64_e32 v[116:117], v[210:211]
	v_mov_b64_e32 v[82:83], v[212:213]
	v_mov_b64_e32 v[84:85], v[214:215]
	ds_write_b128 v53, v[106:109] offset:17408
	ds_write_b128 v53, v[102:105] offset:17424
	s_waitcnt lgkmcnt(5)
	v_mfma_f32_16x16x32_bf16 v[20:23], v[98:101], v[32:35], v[86:89]
	v_lshlrev_b32_e32 v2, 16, v114
	v_and_b32_e32 v3, 0xffff0000, v114
	s_waitcnt lgkmcnt(2)
	v_pk_mul_f32 v[2:3], v[0:1], v[2:3] op_sel_hi:[0,1]
	v_cvt_pk_bf16_f32 v78, v2, v3
	v_lshlrev_b32_e32 v2, 16, v115
	v_and_b32_e32 v3, 0xffff0000, v115
	v_pk_mul_f32 v[2:3], v[0:1], v[2:3] op_sel_hi:[0,1]
	v_cvt_pk_bf16_f32 v79, v2, v3
	v_lshlrev_b32_e32 v2, 16, v116
	v_and_b32_e32 v3, 0xffff0000, v116
	v_pk_mul_f32 v[2:3], v[0:1], v[2:3] op_sel_hi:[0,1]
	v_cvt_pk_bf16_f32 v80, v2, v3
	v_lshlrev_b32_e32 v2, 16, v117
	v_and_b32_e32 v3, 0xffff0000, v117
	v_pk_mul_f32 v[2:3], v[0:1], v[2:3] op_sel_hi:[0,1]
	v_cvt_pk_bf16_f32 v81, v2, v3
	v_lshlrev_b32_e32 v2, 16, v82
	v_and_b32_e32 v3, 0xffff0000, v82
	v_pk_mul_f32 v[2:3], v[0:1], v[2:3] op_sel_hi:[0,1]
	v_cvt_pk_bf16_f32 v82, v2, v3
	v_lshlrev_b32_e32 v2, 16, v83
	v_and_b32_e32 v3, 0xffff0000, v83
	v_pk_mul_f32 v[2:3], v[0:1], v[2:3] op_sel_hi:[0,1]
	v_mfma_f32_16x16x32_bf16 v[32:35], v[98:101], v[110:113], v[90:93]
	v_cvt_pk_bf16_f32 v83, v2, v3
	v_lshlrev_b32_e32 v2, 16, v84
	v_and_b32_e32 v3, 0xffff0000, v84
	v_pk_mul_f32 v[2:3], v[0:1], v[2:3] op_sel_hi:[0,1]
	v_cvt_pk_bf16_f32 v84, v2, v3
	v_lshlrev_b32_e32 v2, 16, v85
	v_and_b32_e32 v3, 0xffff0000, v85
	v_pk_mul_f32 v[2:3], v[0:1], v[2:3] op_sel_hi:[0,1]
	v_cvt_pk_bf16_f32 v85, v2, v3
	ds_write_b128 v53, v[78:81] offset:34816
	ds_write_b128 v53, v[82:85] offset:34832
	s_and_saveexec_b64 s[0:1], s[8:9]
	s_cbranch_execz .LBB0_276
	v_bfe_u32 v2, v0, 16, 1
	v_add3_u32 v0, v0, v2, s28
	v_lshrrev_b32_e32 v0, 16, v0
	v_mov_b32_e32 v2, v1
	v_mov_b32_e32 v3, v1
	ds_write_b128 v66, v[0:3] offset:52224
	ds_write_b128 v66, v[74:77] offset:52240
.LBB0_276:
	s_or_b64 exec, exec, s[0:1]
	s_waitcnt lgkmcnt(0)
	s_barrier
	ds_read_b64_tr_b16 v[78:79], v71 offset:17408
	ds_read_b64_tr_b16 v[80:81], v71 offset:18496
	ds_read_b64_tr_b16 v[82:83], v56 offset:34816
	ds_read_b64_tr_b16 v[86:87], v56 offset:34848
	ds_read_b64_tr_b16 v[90:91], v56 offset:34880
	ds_read_b64_tr_b16 v[94:95], v56 offset:34912
	ds_read_b64_tr_b16 v[84:85], v56 offset:35904
	ds_read_b64_tr_b16 v[88:89], v56 offset:35936
	ds_read_b64_tr_b16 v[92:93], v56 offset:35968
	ds_read_b64_tr_b16 v[96:97], v56 offset:36000
	ds_read_b64_tr_b16 v[98:99], v72 offset:17408
	ds_read_b64_tr_b16 v[100:101], v72 offset:18496
	v_pk_mul_f32 v[38:39], v[38:39], v[50:51] op_sel_hi:[1,0]
	v_pk_mul_f32 v[36:37], v[36:37], v[50:51] op_sel_hi:[1,0]
	v_pk_mul_f32 v[10:11], v[10:11], v[50:51] op_sel_hi:[1,0]
	v_pk_mul_f32 v[8:9], v[8:9], v[50:51] op_sel_hi:[1,0]
	v_pk_mul_f32 v[14:15], v[14:15], v[50:51] op_sel_hi:[1,0]
	v_pk_mul_f32 v[12:13], v[12:13], v[50:51] op_sel_hi:[1,0]
	v_pk_mul_f32 v[18:19], v[18:19], v[50:51] op_sel_hi:[1,0]
	v_pk_mul_f32 v[16:17], v[16:17], v[50:51] op_sel_hi:[1,0]
	s_waitcnt lgkmcnt(5)
	v_mfma_f32_16x16x32_bf16 v[36:39], v[78:81], v[82:85], v[36:39]
	v_mul_f32_e64 v30, v30, v50
	v_mul_f32_e64 v31, v31, v50
	v_pk_mul_f32 v[28:29], v[28:29], v[50:51] op_sel_hi:[1,0]
	v_pk_mul_f32 v[6:7], v[6:7], v[50:51] op_sel_hi:[1,0]
	s_waitcnt lgkmcnt(4)
	v_mfma_f32_16x16x32_bf16 v[8:11], v[78:81], v[86:89], v[8:11]
	v_mul_f32_e64 v4, v4, v50
	v_mul_f32_e64 v5, v5, v50
	v_pk_mul_f32 v[22:23], v[22:23], v[50:51] op_sel_hi:[1,0]
	v_pk_mul_f32 v[20:21], v[20:21], v[50:51] op_sel_hi:[1,0]
	s_waitcnt lgkmcnt(3)
	v_mfma_f32_16x16x32_bf16 v[12:15], v[78:81], v[90:93], v[12:15]
	v_mul_f32_e64 v26, v26, v50
	v_mul_f32_e64 v27, v27, v50
	v_pk_mul_f32 v[24:25], v[24:25], v[50:51] op_sel_hi:[1,0]
	v_mov_b32_e32 v0, s41
	s_waitcnt lgkmcnt(2)
	v_mfma_f32_16x16x32_bf16 v[16:19], v[78:81], v[94:97], v[16:19]
	ds_read_b64_tr_b16 v[84:85], v56 offset:36032
	ds_read_b64_tr_b16 v[82:83], v56 offset:34944
	ds_read_b64_tr_b16 v[86:87], v56 offset:34976
	ds_read_b64_tr_b16 v[90:91], v56 offset:35008
	ds_read_b64_tr_b16 v[94:95], v56 offset:35040
	ds_read_b64_tr_b16 v[88:89], v56 offset:36064
	ds_read_b64_tr_b16 v[92:93], v56 offset:36096
	ds_read_b64_tr_b16 v[96:97], v56 offset:36128
	s_waitcnt lgkmcnt(6)
	v_mfma_f32_16x16x32_bf16 v[82:85], v[78:81], v[82:85], v[28:31]
	s_nop 2
	v_mul_f32_e64 v30, v34, v50
	v_mul_f32_e64 v31, v35, v50
	v_pk_mul_f32 v[28:29], v[32:33], v[50:51] op_sel_hi:[1,0]
	ds_read_b64_tr_b16 v[32:33], v70 offset:52224
	ds_read_b64_tr_b16 v[34:35], v70 offset:52352
	s_waitcnt lgkmcnt(4)
	v_mfma_f32_16x16x32_bf16 v[2:5], v[78:81], v[86:89], v[4:7]
	s_waitcnt lgkmcnt(3)
	v_mfma_f32_16x16x32_bf16 v[20:23], v[78:81], v[90:93], v[20:23]
	ds_read_b64_tr_b16 v[90:91], v67 offset:52224
	ds_read_b64_tr_b16 v[92:93], v67 offset:52352
	v_or_b32_e32 v6, s40, v73
	v_ashrrev_i32_e32 v7, 31, v6
	s_waitcnt lgkmcnt(4)
	v_mfma_f32_16x16x32_bf16 v[86:89], v[78:81], v[94:97], v[28:31]
	s_waitcnt lgkmcnt(2)
	v_mfma_f32_16x16x32_bf16 v[78:81], v[78:81], v[32:35], v[24:27]
	s_nop 2
	ds_read_b64_tr_b16 v[26:27], v59 offset:35904
	ds_read_b64_tr_b16 v[24:25], v59 offset:34816
	ds_read_b64_tr_b16 v[28:29], v59 offset:34848
	ds_read_b64_tr_b16 v[32:33], v59 offset:34880
	ds_read_b64_tr_b16 v[94:95], v59 offset:34912
	ds_read_b64_tr_b16 v[30:31], v59 offset:35936
	ds_read_b64_tr_b16 v[34:35], v59 offset:35968
	ds_read_b64_tr_b16 v[96:97], v59 offset:36000
	s_waitcnt lgkmcnt(6)
; template <bool OUT, bool PASS2>
; __device__ __forceinline__ void ml_block(const Args& a, unsigned char* lds_g, int rowbase, int h, int dir, f32x4 (&st)[9], int tid) {
;     ...
;         {
;             const int t = st_t, pc = st_pc;
;             const float e = eu[64 * c + t];
;             *(v4u*)(Ki + t * ML_STRIDE + 16 * pc) = k0; *(v4u*)(Ki + t * ML_STRIDE + 16 * pc + 8) = k1;
;             if (OUT) { *(v4u*)(Qi + t * ML_STRIDE + 16 * pc) = q0; *(v4u*)(Qi + t * ML_STRIDE + 16 * pc + 8) = q1; }
;             const unsigned vv[8] = {v0.x, v0.y, v0.z, v0.w, v1.x, v1.y, v1.z, v1.w}; unsigned o[8];
; #pragma unroll
;             for (int i = 0; i < 8; ++i) o[i] = pk2(bflo(vv[i]) * e, bfhi(vv[i]) * e);
;             *(v4u*)(Vi + t * ML_STRIDE + 16 * pc) = (v4u){o[0], o[1], o[2], o[3]}; *(v4u*)(Vi + t * ML_STRIDE + 16 * pc + 8) = (v4u){o[4], o[5], o[6], o[7]};
;             if (pc == 0) { *(v4u*)(AUGi + t * 16) = (v4u){f2bf(e), 0u, 0u, 0u}; *(v4u*)(AUGi + t * 16 + 8) = (v4u){0u, 0u, 0u, 0u}; }
;         }
;         WG_BAR();
;         if (ci < 3) ML_LOADC(dir ? 2 - ci : ci + 1);
;         f32x4 X[5]; float hval[4][4];
;         if (OUT) {
;             bf16x8_t qf[4];
; #pragma unroll
;             for (int ks = 0; ks < 4; ++ks) qf[ks] = frag_row(Qi, 16 * ti, 32 * ks, fr, fq);
;             bf16x8_t P[2]; bool pv[2];
; #pragma unroll
;             for (int pp = 0; pp < 2; ++pp) {
;                 f32x4 d[2];
; #pragma unroll
;                 for (int hh = 0; hh < 2; ++hh) { const int si = 2 * pp + hh; d[hh] = (f32x4){0.f, 0.f, 0.f, 0.f};
;                     const bool valid = dir ? (si >= ti) : (si <= ti);
;                     if (valid) {
; #pragma unroll
;                         for (int ks = 0; ks < 4; ++ks) d[hh] = __builtin_amdgcn_mfma_f32_16x16x32_bf16(frag_row(Ki, 16 * si, 32 * ks, fr, fq), qf[ks], d[hh], 0, 0, 0);
;                         if (si == ti) {
; #pragma unroll
;                             for (int r = 0; r < 4; ++r) { const bool keep = dir ? (4 * fq + r >= fr) : (4 * fq + r <= fr); d[hh][r] = keep ? d[hh][r] : 0.f; } } } }
;                 pv[pp] = dir ? (2 * pp + 1 >= ti) : (2 * pp <= ti);
;                 const unsigned p0 = pk2(d[0][0], d[0][1]), p1 = pk2(d[0][2], d[0][3]), p2 = pk2(d[1][0], d[1][1]), p3 = pk2(d[1][2], d[1][3]);
;                 P[pp] = __builtin_bit_cast(bf16x8_t, (v4u){p0, p1, p2, p3});
;             }
	v_mfma_f32_16x16x32_bf16 v[36:39], v[98:101], v[24:27], v[36:39]
	s_waitcnt lgkmcnt(2)
	v_mfma_f32_16x16x32_bf16 v[28:31], v[98:101], v[28:31], v[8:11]
	s_waitcnt lgkmcnt(1)
	v_mfma_f32_16x16x32_bf16 v[24:27], v[98:101], v[32:35], v[12:15]
	s_waitcnt lgkmcnt(0)
	v_mfma_f32_16x16x32_bf16 v[8:11], v[98:101], v[94:97], v[16:19]
	s_nop 0
	ds_read_b64_tr_b16 v[14:15], v59 offset:36032
	ds_read_b64_tr_b16 v[12:13], v59 offset:34944
	ds_read_b64_tr_b16 v[16:17], v59 offset:34976
	ds_read_b64_tr_b16 v[94:95], v59 offset:35008
	ds_read_b64_tr_b16 v[102:103], v59 offset:35040
	ds_read_b64_tr_b16 v[18:19], v59 offset:36064
	ds_read_b64_tr_b16 v[96:97], v59 offset:36096
	ds_read_b64_tr_b16 v[104:105], v59 offset:36128
	s_waitcnt lgkmcnt(6)
	v_mfma_f32_16x16x32_bf16 v[32:35], v[98:101], v[12:15], v[82:85]
	v_lshlrev_b64 v[12:13], 11, v[6:7]
	v_lshl_add_u64 v[110:111], v[48:49], 0, v[12:13]
	s_waitcnt lgkmcnt(2)
	v_mfma_f32_16x16x32_bf16 v[4:7], v[98:101], v[16:19], v[2:5]
	s_nop 2
	v_lshl_add_u64 v[2:3], v[46:47], 0, v[12:13]
	s_waitcnt lgkmcnt(1)
	v_mfma_f32_16x16x32_bf16 v[12:15], v[98:101], v[94:97], v[20:23]
	ds_read_b32 v50, v0 offset:4
	v_add_u32_e32 v0, s42, v69
	s_waitcnt lgkmcnt(1)
	v_mfma_f32_16x16x32_bf16 v[16:19], v[98:101], v[102:105], v[86:89]
	s_nop 2
	s_waitcnt lgkmcnt(0)
	s_barrier
	ds_read_b32 v0, v0
	v_mfma_f32_16x16x32_bf16 v[20:23], v[98:101], v[90:93], v[78:81]
	s_waitcnt vmcnt(6)
	v_mov_b64_e32 v[82:83], v[216:217]
	v_mov_b64_e32 v[84:85], v[218:219]
	v_mov_b64_e32 v[106:107], v[220:221]
	v_mov_b64_e32 v[108:109], v[222:223]
	v_mov_b64_e32 v[94:95], v[224:225]
	v_mov_b64_e32 v[96:97], v[226:227]
	v_mov_b64_e32 v[86:87], v[228:229]
	v_mov_b64_e32 v[88:89], v[230:231]
	ds_write_b128 v53, v[106:109] offset:17408
	ds_write_b128 v53, v[82:85] offset:17424
	v_lshlrev_b32_e32 v2, 16, v94
	v_and_b32_e32 v3, 0xffff0000, v94
	s_waitcnt lgkmcnt(2)
	v_pk_mul_f32 v[2:3], v[0:1], v[2:3] op_sel_hi:[0,1]
	v_cvt_pk_bf16_f32 v78, v2, v3
	v_lshlrev_b32_e32 v2, 16, v95
	v_and_b32_e32 v3, 0xffff0000, v95
	v_pk_mul_f32 v[2:3], v[0:1], v[2:3] op_sel_hi:[0,1]
	v_cvt_pk_bf16_f32 v79, v2, v3
	v_lshlrev_b32_e32 v2, 16, v96
	v_and_b32_e32 v3, 0xffff0000, v96
	v_pk_mul_f32 v[2:3], v[0:1], v[2:3] op_sel_hi:[0,1]
	v_cvt_pk_bf16_f32 v80, v2, v3
	v_lshlrev_b32_e32 v2, 16, v97
	v_and_b32_e32 v3, 0xffff0000, v97
	v_pk_mul_f32 v[2:3], v[0:1], v[2:3] op_sel_hi:[0,1]
	v_cvt_pk_bf16_f32 v81, v2, v3
	v_lshlrev_b32_e32 v2, 16, v86
	v_and_b32_e32 v3, 0xffff0000, v86
	v_pk_mul_f32 v[2:3], v[0:1], v[2:3] op_sel_hi:[0,1]
	v_cvt_pk_bf16_f32 v82, v2, v3
	v_lshlrev_b32_e32 v2, 16, v87
	v_and_b32_e32 v3, 0xffff0000, v87
	v_pk_mul_f32 v[2:3], v[0:1], v[2:3] op_sel_hi:[0,1]
	v_cvt_pk_bf16_f32 v83, v2, v3
	v_lshlrev_b32_e32 v2, 16, v88
	v_and_b32_e32 v3, 0xffff0000, v88
	v_pk_mul_f32 v[2:3], v[0:1], v[2:3] op_sel_hi:[0,1]
	v_cvt_pk_bf16_f32 v84, v2, v3
	v_lshlrev_b32_e32 v2, 16, v89
	v_and_b32_e32 v3, 0xffff0000, v89
	v_pk_mul_f32 v[2:3], v[0:1], v[2:3] op_sel_hi:[0,1]
	v_cvt_pk_bf16_f32 v85, v2, v3
	ds_write_b128 v53, v[78:81] offset:34816
	ds_write_b128 v53, v[82:85] offset:34832
	s_and_saveexec_b64 s[0:1], s[8:9]
	s_cbranch_execz .LBB0_278
	v_bfe_u32 v2, v0, 16, 1
	v_add3_u32 v0, v0, v2, s28
	v_lshrrev_b32_e32 v0, 16, v0
	v_mov_b32_e32 v2, v1
	v_mov_b32_e32 v3, v1
	ds_write_b128 v66, v[0:3] offset:52224
	ds_write_b128 v66, v[74:77] offset:52240
; template <bool OUT, bool PASS2>
; __device__ __forceinline__ void ml_block(const Args& a, unsigned char* lds_g, int rowbase, int h, int dir, f32x4 (&st)[9], int tid) {
;     ...
;         {
;             const int t = st_t, pc = st_pc;
;             const float e = eu[64 * c + t];
;             *(v4u*)(Ki + t * ML_STRIDE + 16 * pc) = k0; *(v4u*)(Ki + t * ML_STRIDE + 16 * pc + 8) = k1;
;             if (OUT) { *(v4u*)(Qi + t * ML_STRIDE + 16 * pc) = q0; *(v4u*)(Qi + t * ML_STRIDE + 16 * pc + 8) = q1; }
;             const unsigned vv[8] = {v0.x, v0.y, v0.z, v0.w, v1.x, v1.y, v1.z, v1.w}; unsigned o[8];
; #pragma unroll
;             for (int i = 0; i < 8; ++i) o[i] = pk2(bflo(vv[i]) * e, bfhi(vv[i]) * e);
;             *(v4u*)(Vi + t * ML_STRIDE + 16 * pc) = (v4u){o[0], o[1], o[2], o[3]}; *(v4u*)(Vi + t * ML_STRIDE + 16 * pc + 8) = (v4u){o[4], o[5], o[6], o[7]};
;             if (pc == 0) { *(v4u*)(AUGi + t * 16) = (v4u){f2bf(e), 0u, 0u, 0u}; *(v4u*)(AUGi + t * 16 + 8) = (v4u){0u, 0u, 0u, 0u}; }
;         }
;         WG_BAR();
;         if (ci < 3) ML_LOADC(dir ? 2 - ci : ci + 1);
;         f32x4 X[5]; float hval[4][4];
;         if (OUT) {
;             bf16x8_t qf[4];
; #pragma unroll
;             for (int ks = 0; ks < 4; ++ks) qf[ks] = frag_row(Qi, 16 * ti, 32 * ks, fr, fq);
;             bf16x8_t P[2]; bool pv[2];
; #pragma unroll
;             for (int pp = 0; pp < 2; ++pp) {
;                 f32x4 d[2];
; #pragma unroll
;                 for (int hh = 0; hh < 2; ++hh) { const int si = 2 * pp + hh; d[hh] = (f32x4){0.f, 0.f, 0.f, 0.f};
;                     const bool valid = dir ? (si >= ti) : (si <= ti);
;                     if (valid) {
; #pragma unroll
;                         for (int ks = 0; ks < 4; ++ks) d[hh] = __builtin_amdgcn_mfma_f32_16x16x32_bf16(frag_row(Ki, 16 * si, 32 * ks, fr, fq), qf[ks], d[hh], 0, 0, 0);
;                         if (si == ti) {
; #pragma unroll
;                             for (int r = 0; r < 4; ++r) { const bool keep = dir ? (4 * fq + r >= fr) : (4 * fq + r <= fr); d[hh][r] = keep ? d[hh][r] : 0.f; } } } }
;                 pv[pp] = dir ? (2 * pp + 1 >= ti) : (2 * pp <= ti);
;                 const unsigned p0 = pk2(d[0][0], d[0][1]), p1 = pk2(d[0][2], d[0][3]), p2 = pk2(d[1][0], d[1][1]), p3 = pk2(d[1][2], d[1][3]);
;                 P[pp] = __builtin_bit_cast(bf16x8_t, (v4u){p0, p1, p2, p3});
;             }
.LBB0_278:
	s_or_b64 exec, exec, s[0:1]
	s_waitcnt lgkmcnt(0)
	s_barrier
	ds_read_b64_tr_b16 v[78:79], v71 offset:17408
	ds_read_b64_tr_b16 v[80:81], v71 offset:18496
	ds_read_b64_tr_b16 v[82:83], v56 offset:34816
	ds_read_b64_tr_b16 v[86:87], v56 offset:34848
	ds_read_b64_tr_b16 v[90:91], v56 offset:34880
	ds_read_b64_tr_b16 v[94:95], v56 offset:34912
	ds_read_b64_tr_b16 v[84:85], v56 offset:35904
	ds_read_b64_tr_b16 v[88:89], v56 offset:35936
	ds_read_b64_tr_b16 v[92:93], v56 offset:35968
	ds_read_b64_tr_b16 v[96:97], v56 offset:36000
	ds_read_b64_tr_b16 v[98:99], v72 offset:17408
	ds_read_b64_tr_b16 v[100:101], v72 offset:18496
	v_pk_mul_f32 v[38:39], v[38:39], v[50:51] op_sel_hi:[1,0]
	v_pk_mul_f32 v[36:37], v[36:37], v[50:51] op_sel_hi:[1,0]
	v_pk_mul_f32 v[30:31], v[30:31], v[50:51] op_sel_hi:[1,0]
	v_pk_mul_f32 v[28:29], v[28:29], v[50:51] op_sel_hi:[1,0]
	v_pk_mul_f32 v[26:27], v[26:27], v[50:51] op_sel_hi:[1,0]
	v_pk_mul_f32 v[24:25], v[24:25], v[50:51] op_sel_hi:[1,0]
	v_pk_mul_f32 v[10:11], v[10:11], v[50:51] op_sel_hi:[1,0]
	v_pk_mul_f32 v[8:9], v[8:9], v[50:51] op_sel_hi:[1,0]
	s_waitcnt lgkmcnt(5)
	v_mfma_f32_16x16x32_bf16 v[36:39], v[78:81], v[82:85], v[36:39]
	v_mul_f32_e64 v34, v34, v50
	v_mul_f32_e64 v35, v35, v50
	v_pk_mul_f32 v[32:33], v[32:33], v[50:51] op_sel_hi:[1,0]
	v_pk_mul_f32 v[6:7], v[6:7], v[50:51] op_sel_hi:[1,0]
	s_waitcnt lgkmcnt(4)
	v_mfma_f32_16x16x32_bf16 v[28:31], v[78:81], v[86:89], v[28:31]
	v_mul_f32_e64 v4, v4, v50
	v_mul_f32_e64 v5, v5, v50
	v_pk_mul_f32 v[14:15], v[14:15], v[50:51] op_sel_hi:[1,0]
	v_pk_mul_f32 v[12:13], v[12:13], v[50:51] op_sel_hi:[1,0]
	s_waitcnt lgkmcnt(3)
	v_mfma_f32_16x16x32_bf16 v[24:27], v[78:81], v[90:93], v[24:27]
	v_mul_f32_e64 v18, v18, v50
	v_mul_f32_e64 v19, v19, v50
	v_pk_mul_f32 v[16:17], v[16:17], v[50:51] op_sel_hi:[1,0]
	v_pk_mul_f32 v[22:23], v[22:23], v[50:51] op_sel_hi:[1,0]
	s_waitcnt lgkmcnt(2)
	v_mfma_f32_16x16x32_bf16 v[8:11], v[78:81], v[94:97], v[8:11]
	ds_read_b64_tr_b16 v[84:85], v56 offset:36032
	ds_read_b64_tr_b16 v[82:83], v56 offset:34944
	ds_read_b64_tr_b16 v[86:87], v56 offset:34976
	ds_read_b64_tr_b16 v[90:91], v56 offset:35008
	ds_read_b64_tr_b16 v[94:95], v56 offset:35040
	ds_read_b64_tr_b16 v[88:89], v56 offset:36064
	ds_read_b64_tr_b16 v[92:93], v56 offset:36096
	ds_read_b64_tr_b16 v[96:97], v56 offset:36128
	v_pk_mul_f32 v[20:21], v[20:21], v[50:51] op_sel_hi:[1,0]
	v_mov_b32_e32 v0, s44
	s_waitcnt lgkmcnt(6)
	v_mfma_f32_16x16x32_bf16 v[32:35], v[78:81], v[82:85], v[32:35]
	ds_read_b64_tr_b16 v[82:83], v70 offset:52224
	ds_read_b64_tr_b16 v[84:85], v70 offset:52352
	s_waitcnt lgkmcnt(4)
	v_mfma_f32_16x16x32_bf16 v[2:5], v[78:81], v[86:89], v[4:7]
	ds_read_b64_tr_b16 v[86:87], v67 offset:52224
	ds_read_b64_tr_b16 v[88:89], v67 offset:52352
	s_nop 0
	v_or_b32_e32 v6, s43, v73
	s_waitcnt lgkmcnt(5)
	v_mfma_f32_16x16x32_bf16 v[12:15], v[78:81], v[90:93], v[12:15]
	v_ashrrev_i32_e32 v7, 31, v6
	s_waitcnt lgkmcnt(4)
	v_mfma_f32_16x16x32_bf16 v[16:19], v[78:81], v[94:97], v[16:19]
	s_waitcnt lgkmcnt(2)
	v_mfma_f32_16x16x32_bf16 v[20:23], v[78:81], v[82:85], v[20:23]
	ds_read_b64_tr_b16 v[80:81], v59 offset:35904
	ds_read_b64_tr_b16 v[78:79], v59 offset:34816
	ds_read_b64_tr_b16 v[82:83], v59 offset:34848
	ds_read_b64_tr_b16 v[90:91], v59 offset:34880
	ds_read_b64_tr_b16 v[94:95], v59 offset:34912
	ds_read_b64_tr_b16 v[84:85], v59 offset:35936
	ds_read_b64_tr_b16 v[92:93], v59 offset:35968
	ds_read_b64_tr_b16 v[96:97], v59 offset:36000
	s_waitcnt lgkmcnt(6)
	v_mfma_f32_16x16x32_bf16 v[36:39], v[98:101], v[78:81], v[36:39]
	s_waitcnt lgkmcnt(2)
	v_mfma_f32_16x16x32_bf16 v[28:31], v[98:101], v[82:85], v[28:31]
	s_waitcnt lgkmcnt(1)
	v_mfma_f32_16x16x32_bf16 v[24:27], v[98:101], v[90:93], v[24:27]
	s_waitcnt lgkmcnt(0)
	v_mfma_f32_16x16x32_bf16 v[8:11], v[98:101], v[94:97], v[8:11]
	ds_read_b64_tr_b16 v[80:81], v59 offset:36032
	ds_read_b64_tr_b16 v[78:79], v59 offset:34944
	ds_read_b64_tr_b16 v[82:83], v59 offset:34976
	ds_read_b64_tr_b16 v[90:91], v59 offset:35008
	ds_read_b64_tr_b16 v[94:95], v59 offset:35040
	ds_read_b64_tr_b16 v[84:85], v59 offset:36064
	ds_read_b64_tr_b16 v[92:93], v59 offset:36096
	ds_read_b64_tr_b16 v[96:97], v59 offset:36128
	s_waitcnt lgkmcnt(6)
	v_mfma_f32_16x16x32_bf16 v[32:35], v[98:101], v[78:81], v[32:35]
	v_lshlrev_b64 v[78:79], 11, v[6:7]
	v_lshl_add_u64 v[102:103], v[48:49], 0, v[78:79]
	s_waitcnt lgkmcnt(2)
	v_mfma_f32_16x16x32_bf16 v[4:7], v[98:101], v[82:85], v[2:5]
	s_nop 2
	v_lshl_add_u64 v[2:3], v[46:47], 0, v[78:79]
	s_waitcnt lgkmcnt(1)
	v_mfma_f32_16x16x32_bf16 v[12:15], v[98:101], v[90:93], v[12:15]
	ds_read_b32 v50, v0 offset:8
	v_add_u32_e32 v0, s45, v69
	s_waitcnt lgkmcnt(1)
	v_mfma_f32_16x16x32_bf16 v[16:19], v[98:101], v[94:97], v[16:19]
	s_waitcnt lgkmcnt(0)
	s_barrier
	ds_read_b32 v0, v0
	v_mfma_f32_16x16x32_bf16 v[20:23], v[98:101], v[86:89], v[20:23]
	s_waitcnt vmcnt(2)
	v_mov_b64_e32 v[78:79], v[232:233]
	v_mov_b64_e32 v[80:81], v[234:235]
	v_mov_b64_e32 v[82:83], v[236:237]
	v_mov_b64_e32 v[84:85], v[238:239]
	v_mov_b64_e32 v[90:91], v[240:241]
	v_mov_b64_e32 v[92:93], v[242:243]
	v_mov_b64_e32 v[94:95], v[244:245]
	v_mov_b64_e32 v[96:97], v[246:247]
	ds_write_b128 v53, v[82:85] offset:17408
	ds_write_b128 v53, v[78:81] offset:17424
	v_lshlrev_b32_e32 v2, 16, v90
	v_and_b32_e32 v3, 0xffff0000, v90
	s_waitcnt lgkmcnt(2)
	v_pk_mul_f32 v[2:3], v[0:1], v[2:3] op_sel_hi:[0,1]
	v_cvt_pk_bf16_f32 v78, v2, v3
	v_lshlrev_b32_e32 v2, 16, v91
	v_and_b32_e32 v3, 0xffff0000, v91
	v_pk_mul_f32 v[2:3], v[0:1], v[2:3] op_sel_hi:[0,1]
	v_cvt_pk_bf16_f32 v79, v2, v3
	v_lshlrev_b32_e32 v2, 16, v92
	v_and_b32_e32 v3, 0xffff0000, v92
	v_pk_mul_f32 v[2:3], v[0:1], v[2:3] op_sel_hi:[0,1]
	v_cvt_pk_bf16_f32 v80, v2, v3
	v_lshlrev_b32_e32 v2, 16, v93
	v_and_b32_e32 v3, 0xffff0000, v93
	v_pk_mul_f32 v[2:3], v[0:1], v[2:3] op_sel_hi:[0,1]
	v_cvt_pk_bf16_f32 v81, v2, v3
	v_lshlrev_b32_e32 v2, 16, v94
	v_and_b32_e32 v3, 0xffff0000, v94
	v_pk_mul_f32 v[2:3], v[0:1], v[2:3] op_sel_hi:[0,1]
	v_cvt_pk_bf16_f32 v82, v2, v3
	v_lshlrev_b32_e32 v2, 16, v95
	v_and_b32_e32 v3, 0xffff0000, v95
	v_pk_mul_f32 v[2:3], v[0:1], v[2:3] op_sel_hi:[0,1]
	v_cvt_pk_bf16_f32 v83, v2, v3
	v_lshlrev_b32_e32 v2, 16, v96
	v_and_b32_e32 v3, 0xffff0000, v96
	v_pk_mul_f32 v[2:3], v[0:1], v[2:3] op_sel_hi:[0,1]
	v_cvt_pk_bf16_f32 v84, v2, v3
	v_lshlrev_b32_e32 v2, 16, v97
	v_and_b32_e32 v3, 0xffff0000, v97
	v_pk_mul_f32 v[2:3], v[0:1], v[2:3] op_sel_hi:[0,1]
	v_cvt_pk_bf16_f32 v85, v2, v3
	ds_write_b128 v53, v[78:81] offset:34816
	ds_write_b128 v53, v[82:85] offset:34832
	s_and_saveexec_b64 s[0:1], s[8:9]
	s_cbranch_execz .LBB0_280
	v_bfe_u32 v2, v0, 16, 1
	v_add3_u32 v0, v0, v2, s28
	v_lshrrev_b32_e32 v0, 16, v0
	v_mov_b32_e32 v2, v1
	v_mov_b32_e32 v3, v1
	ds_write_b128 v66, v[0:3] offset:52224
	ds_write_b128 v66, v[74:77] offset:52240
